# gate unit: selection-stage LDS reads batched (8 wide reads instead of 32 dependent ds_read_b32) and scoring loop reads one chunk ahead into a second register set; on top of the kmean/gate-staging/barr
# speedup vs baseline: 1.0045x; 1.0045x over previous
.LBB0_485:
	ds_read_b128 v[80:83], v2
	ds_read_b128 v[84:87], v2 offset:64
	ds_read_b128 v[88:91], v2 offset:16
	ds_read_b128 v[92:95], v2 offset:80
	ds_read_b128 v[98:101], v2 offset:128
	ds_read_b128 v[102:105], v2 offset:192
	ds_read_b128 v[106:109], v2 offset:144
	ds_read_b128 v[110:113], v2 offset:208
	s_waitcnt lgkmcnt(7)
	v_mov_b32_e32 v96, v80
	s_waitcnt lgkmcnt(6)
	v_mov_b32_e32 v97, v84
	v_mov_b32_e32 v84, v81
	v_pk_mul_f32 v[80:81], v[84:85], v[10:11]
	v_mov_b32_e32 v84, v82
	v_pk_fma_f32 v[80:81], v[96:97], v[8:9], v[80:81]
	v_mov_b32_e32 v85, v86
	v_pk_fma_f32 v[80:81], v[84:85], v[12:13], v[80:81]
	v_mov_b32_e32 v86, v83
	v_pk_fma_f32 v[80:81], v[86:87], v[14:15], v[80:81]
	s_waitcnt lgkmcnt(5)
	v_mov_b32_e32 v82, v88
	s_waitcnt lgkmcnt(4)
	v_mov_b32_e32 v83, v92
	v_pk_fma_f32 v[80:81], v[82:83], v[16:17], v[80:81]
	v_mov_b32_e32 v92, v89
	v_pk_fma_f32 v[80:81], v[92:93], v[18:19], v[80:81]
	v_mov_b32_e32 v82, v90
	v_mov_b32_e32 v83, v94
	v_pk_fma_f32 v[80:81], v[82:83], v[20:21], v[80:81]
	v_mov_b32_e32 v94, v91
	v_pk_fma_f32 v[88:89], v[94:95], v[22:23], v[80:81]
	v_add_f32_e32 v79, 0, v88
	v_add_f32_e32 v79, v79, v89
	ds_read_b128 v[80:83], v2 offset:256
	ds_read_b128 v[84:87], v2 offset:320
	ds_read_b128 v[88:91], v2 offset:272
	ds_read_b128 v[92:95], v2 offset:336
	s_waitcnt lgkmcnt(7)
	v_mov_b32_e32 v96, v98
	s_waitcnt lgkmcnt(6)
	v_mov_b32_e32 v97, v102
	v_mov_b32_e32 v102, v99
	v_pk_mul_f32 v[98:99], v[102:103], v[26:27]
	v_mov_b32_e32 v102, v100
	v_pk_fma_f32 v[98:99], v[96:97], v[24:25], v[98:99]
	v_mov_b32_e32 v103, v104
	v_pk_fma_f32 v[98:99], v[102:103], v[28:29], v[98:99]
	v_mov_b32_e32 v104, v101
	v_pk_fma_f32 v[98:99], v[104:105], v[30:31], v[98:99]
	s_waitcnt lgkmcnt(5)
	v_mov_b32_e32 v100, v106
	s_waitcnt lgkmcnt(4)
	v_mov_b32_e32 v101, v110
	v_pk_fma_f32 v[98:99], v[100:101], v[32:33], v[98:99]
	v_mov_b32_e32 v110, v107
	v_pk_fma_f32 v[98:99], v[110:111], v[34:35], v[98:99]
	v_mov_b32_e32 v100, v108
	v_mov_b32_e32 v101, v112
	v_pk_fma_f32 v[98:99], v[100:101], v[36:37], v[98:99]
	v_mov_b32_e32 v112, v109
	v_pk_fma_f32 v[106:107], v[112:113], v[38:39], v[98:99]
	v_add_f32_e32 v79, v79, v106
	v_add_f32_e32 v79, v79, v107
	ds_read_b128 v[98:101], v2 offset:384
	ds_read_b128 v[102:105], v2 offset:448
	ds_read_b128 v[106:109], v2 offset:400
	ds_read_b128 v[110:113], v2 offset:464
	s_waitcnt lgkmcnt(7)
	v_mov_b32_e32 v96, v80
	s_waitcnt lgkmcnt(6)
	v_mov_b32_e32 v97, v84
	v_mov_b32_e32 v84, v81
	v_pk_mul_f32 v[80:81], v[84:85], v[42:43]
	v_mov_b32_e32 v84, v82
	v_pk_fma_f32 v[80:81], v[96:97], v[40:41], v[80:81]
	v_mov_b32_e32 v85, v86
	v_pk_fma_f32 v[80:81], v[84:85], v[44:45], v[80:81]
	v_mov_b32_e32 v86, v83
	v_pk_fma_f32 v[80:81], v[86:87], v[46:47], v[80:81]
	s_waitcnt lgkmcnt(5)
	v_mov_b32_e32 v82, v88
	s_waitcnt lgkmcnt(4)
	v_mov_b32_e32 v83, v92
	v_pk_fma_f32 v[80:81], v[82:83], v[48:49], v[80:81]
	v_mov_b32_e32 v92, v89
	v_pk_fma_f32 v[80:81], v[92:93], v[50:51], v[80:81]
	v_mov_b32_e32 v82, v90
	v_mov_b32_e32 v83, v94
	v_pk_fma_f32 v[80:81], v[82:83], v[52:53], v[80:81]
	v_mov_b32_e32 v94, v91
	v_pk_fma_f32 v[88:89], v[94:95], v[54:55], v[80:81]
	v_add_f32_e32 v79, v79, v88
	v_add_f32_e32 v79, v79, v89
	s_waitcnt lgkmcnt(3)
	v_mov_b32_e32 v96, v98
	s_waitcnt lgkmcnt(2)
	v_mov_b32_e32 v97, v102
	v_mov_b32_e32 v102, v99
	v_pk_mul_f32 v[98:99], v[102:103], v[58:59]
	v_mov_b32_e32 v102, v100
	v_pk_fma_f32 v[98:99], v[96:97], v[56:57], v[98:99]
	v_mov_b32_e32 v103, v104
	v_pk_fma_f32 v[98:99], v[102:103], v[60:61], v[98:99]
	v_mov_b32_e32 v104, v101
	v_pk_fma_f32 v[98:99], v[104:105], v[62:63], v[98:99]
	s_waitcnt lgkmcnt(1)
	v_mov_b32_e32 v100, v106
	s_waitcnt lgkmcnt(0)
	v_mov_b32_e32 v101, v110
	v_pk_fma_f32 v[98:99], v[100:101], v[64:65], v[98:99]
	v_mov_b32_e32 v110, v107
	v_pk_fma_f32 v[98:99], v[110:111], v[66:67], v[98:99]
	v_mov_b32_e32 v100, v108
	v_mov_b32_e32 v101, v112
	v_pk_fma_f32 v[98:99], v[100:101], v[68:69], v[98:99]
	v_mov_b32_e32 v112, v109
	v_pk_fma_f32 v[98:99], v[112:113], v[70:71], v[98:99]
	v_mov_b32_e32 v82, v74
	v_add_f32_e32 v79, v79, v98
	v_add_f32_e32 v79, v79, v99
	ds_bpermute_b32 v80, v7, v79
	v_mov_b32_e32 v81, s7
	s_waitcnt lgkmcnt(0)
	v_add_f32_e32 v79, v79, v80
	v_cmp_ngt_f32_e32 vcc, v79, v74
	v_mov_b32_e32 v80, v73
	s_and_saveexec_b64 s[0:1], vcc
	s_cbranch_execz .LBB0_491
	v_cmp_ngt_f32_e32 vcc, v79, v75
	v_mov_b32_e32 v80, s7
	s_and_saveexec_b64 s[8:9], vcc
	s_cbranch_execz .LBB0_490
	v_cmp_gt_f32_e32 vcc, v79, v78
	s_and_saveexec_b64 s[10:11], vcc
	v_mov_b32_e32 v77, s7
	v_mov_b32_e32 v78, v79
	s_or_b64 exec, exec, s[10:11]
	v_mov_b32_e32 v79, v75
	v_mov_b32_e32 v75, v78
	v_mov_b32_e32 v80, v76
	v_mov_b32_e32 v76, v77
